# speedup vs baseline: 1.0275x; 1.0124x over previous
.LBB1_8:
	s_or_b64 exec, exec, s[4:5]
	v_add_u32_e32 v10, v172, v2
	s_waitcnt vmcnt(1) lgkmcnt(0)
	s_barrier
	ds_read_b128 v[18:21], v10 offset:256
	ds_read_b128 v[22:25], v10 offset:288
	ds_read_b128 v[82:85], v10 offset:320
	ds_read_b128 v[86:89], v10 offset:352
	ds_read_b128 v[74:77], v10 offset:384
	ds_read_b128 v[78:81], v10 offset:416
	ds_read_b128 v[2:5], v213 offset:32768
	ds_read_b128 v[6:9], v213 offset:0
	ds_read_b128 v[66:69], v10 offset:448
	ds_read_b128 v[70:73], v10 offset:480
	ds_read_b128 v[10:13], v213 offset:1024
	s_waitcnt lgkmcnt(3)
	v_pk_mul_f32 v[26:27], v[8:9], v[20:21]
	v_pk_mul_f32 v[28:29], v[6:7], v[18:19]
	ds_read_b128 v[14:17], v213 offset:8192
	s_waitcnt lgkmcnt(1)
	v_pk_mul_f32 v[12:13], v[12:13], v[24:25]
	v_pk_mul_f32 v[10:11], v[10:11], v[22:23]
	v_pk_fma_f32 v[30:31], v[8:9], v[20:21], v[12:13]
	v_pk_fma_f32 v[32:33], v[6:7], v[18:19], v[10:11]
	v_cvt_pk_bf16_f32 v9, v12, v13
	v_cvt_pk_bf16_f32 v7, v26, v27
	v_cvt_pk_bf16_f32 v8, v10, v11
	v_cvt_pk_bf16_f32 v6, v28, v29
	ds_read_b128 v[10:13], v213 offset:33792
	s_nop 0
	v_mfma_f32_32x32x16_bf16 v[34:49], v[2:5], v[6:9], 0
	ds_read_b128 v[6:9], v213 offset:9216
	s_waitcnt lgkmcnt(2)
	v_mul_f32_e32 v26, v16, v20
	v_mul_f32_e32 v27, v17, v21
	v_pk_mul_f32 v[50:51], v[14:15], v[18:19]
	s_mov_b32 s4, 0x3727c5ac
	s_waitcnt lgkmcnt(0)
	v_pk_mul_f32 v[8:9], v[8:9], v[24:25]
	v_pk_mul_f32 v[28:29], v[6:7], v[22:23]
	v_pk_fma_f32 v[90:91], v[16:17], v[20:21], v[8:9]
	v_pk_fma_f32 v[92:93], v[14:15], v[18:19], v[28:29]
	ds_read_b128 v[14:17], v213 offset:2048
	v_cvt_pk_bf16_f32 v9, v8, v9
	v_cvt_pk_bf16_f32 v7, v26, v27
	v_cvt_pk_bf16_f32 v8, v28, v29
	ds_read_b128 v[26:29], v213 offset:3072
	v_cvt_pk_bf16_f32 v6, v50, v51
	s_waitcnt lgkmcnt(1)
	v_pk_mul_f32 v[94:95], v[14:15], v[82:83]
	s_mov_b32 s0, 0x3c800000
	v_mfma_f32_32x32x16_bf16 v[50:65], v[2:5], v[6:9], 0
	v_mul_f32_e32 v2, v16, v84
	v_mul_f32_e32 v3, v17, v85
	s_waitcnt lgkmcnt(0)
	v_mul_f32_e32 v4, v28, v88
	v_mul_f32_e32 v5, v29, v89
	v_pk_mul_f32 v[6:7], v[26:27], v[86:87]
	v_pk_fma_f32 v[8:9], v[16:17], v[84:85], v[4:5]
	v_cvt_pk_bf16_f32 v3, v2, v3
	v_pk_fma_f32 v[14:15], v[14:15], v[82:83], v[6:7]
	v_pk_add_f32 v[26:27], v[8:9], v[30:31]
	v_cvt_pk_bf16_f32 v5, v4, v5
	v_cvt_pk_bf16_f32 v4, v6, v7
	ds_read_b128 v[6:9], v213 offset:10240
	v_pk_add_f32 v[28:29], v[14:15], v[32:33]
	ds_read_b128 v[14:17], v213 offset:11264
	v_cvt_pk_bf16_f32 v2, v94, v95
	s_waitcnt lgkmcnt(1)
	v_pk_mul_f32 v[30:31], v[6:7], v[82:83]
	v_mov_b64_e32 v[152:153], s[4:5]
	v_mfma_f32_32x32x16_bf16 v[34:49], v[10:13], v[2:5], v[34:49]
	v_mul_f32_e32 v2, v8, v84
	v_mul_f32_e32 v3, v9, v85
	s_waitcnt lgkmcnt(0)
	v_mul_f32_e32 v4, v16, v88
	v_mul_f32_e32 v5, v17, v89
	v_pk_mul_f32 v[14:15], v[14:15], v[86:87]
	v_pk_fma_f32 v[8:9], v[8:9], v[84:85], v[4:5]
	v_pk_fma_f32 v[6:7], v[6:7], v[82:83], v[14:15]
	v_cvt_pk_bf16_f32 v5, v4, v5
	v_cvt_pk_bf16_f32 v3, v2, v3
	v_cvt_pk_bf16_f32 v4, v14, v15
	v_pk_add_f32 v[32:33], v[8:9], v[90:91]
	v_pk_add_f32 v[90:91], v[6:7], v[92:93]
	ds_read_b128 v[6:9], v213 offset:34816
	ds_read_b128 v[14:17], v213 offset:4096
	v_cvt_pk_bf16_f32 v2, v30, v31
	s_mov_b32 s13, 0
	s_mov_b64 s[6:7], 0
	v_mfma_f32_32x32x16_bf16 v[50:65], v[10:13], v[2:5], v[50:65]
	ds_read_b128 v[2:5], v213 offset:5120
	ds_read_b128 v[10:13], v213 offset:12288
	s_waitcnt lgkmcnt(2)
	v_pk_mul_f32 v[30:31], v[16:17], v[76:77]
	v_pk_mul_f32 v[92:93], v[14:15], v[74:75]
	s_waitcnt lgkmcnt(1)
	v_pk_mul_f32 v[4:5], v[4:5], v[80:81]
	v_pk_mul_f32 v[94:95], v[2:3], v[78:79]
	v_pk_fma_f32 v[2:3], v[16:17], v[76:77], v[4:5]
	v_cvt_pk_bf16_f32 v5, v4, v5
	v_pk_add_f32 v[96:97], v[2:3], v[26:27]
	v_cvt_pk_bf16_f32 v3, v30, v31
	v_cvt_pk_bf16_f32 v4, v94, v95
	v_cvt_pk_bf16_f32 v2, v92, v93
	v_pk_fma_f32 v[14:15], v[14:15], v[74:75], v[94:95]
	s_waitcnt lgkmcnt(0)
	v_pk_mul_f32 v[30:31], v[10:11], v[74:75]
	v_mfma_f32_32x32x16_bf16 v[34:49], v[6:9], v[2:5], v[34:49]
	ds_read_b128 v[2:5], v213 offset:13312
	v_add_f32_e32 v98, v14, v28
	v_add_f32_e32 v99, v15, v29
	ds_read_b128 v[14:17], v213 offset:35840
	v_pk_mul_f32 v[26:27], v[12:13], v[76:77]
	s_waitcnt lgkmcnt(1)
	v_pk_mul_f32 v[4:5], v[4:5], v[80:81]
	v_pk_mul_f32 v[28:29], v[2:3], v[78:79]
	v_pk_fma_f32 v[2:3], v[12:13], v[76:77], v[4:5]
	v_pk_fma_f32 v[10:11], v[10:11], v[74:75], v[28:29]
	v_pk_add_f32 v[32:33], v[2:3], v[32:33]
	v_pk_add_f32 v[92:93], v[10:11], v[90:91]
	ds_read_b128 v[10:13], v213 offset:6144
	v_cvt_pk_bf16_f32 v5, v4, v5
	v_cvt_pk_bf16_f32 v3, v26, v27
	v_cvt_pk_bf16_f32 v4, v28, v29
	ds_read_b128 v[26:29], v213 offset:7168
	v_cvt_pk_bf16_f32 v2, v30, v31
	s_waitcnt lgkmcnt(1)
	v_pk_mul_f32 v[30:31], v[10:11], v[66:67]
	v_mfma_f32_32x32x16_bf16 v[50:65], v[6:9], v[2:5], v[50:65]
	v_mul_f32_e32 v2, v12, v68
	v_mul_f32_e32 v3, v13, v69
	s_waitcnt lgkmcnt(0)
	v_mul_f32_e32 v4, v28, v72
	v_mul_f32_e32 v5, v29, v73
	v_pk_mul_f32 v[6:7], v[26:27], v[70:71]
	v_pk_fma_f32 v[8:9], v[12:13], v[68:69], v[4:5]
	v_cvt_pk_bf16_f32 v3, v2, v3
	v_pk_fma_f32 v[10:11], v[10:11], v[66:67], v[6:7]
	v_pk_add_f32 v[94:95], v[8:9], v[96:97]
	v_cvt_pk_bf16_f32 v5, v4, v5
	v_cvt_pk_bf16_f32 v4, v6, v7
	ds_read_b128 v[6:9], v213 offset:14336
	v_pk_add_f32 v[96:97], v[10:11], v[98:99]
	ds_read_b128 v[10:13], v213 offset:15360
	v_cvt_pk_bf16_f32 v2, v30, v31
	s_waitcnt lgkmcnt(1)
	v_pk_mul_f32 v[30:31], v[6:7], v[66:67]
	v_mfma_f32_32x32x16_bf16 v[34:49], v[14:17], v[2:5], v[34:49]
	s_waitcnt lgkmcnt(0)
	v_mul_f32_e32 v10, v10, v70
	v_mul_f32_e32 v11, v11, v71
	v_mul_f32_e32 v2, v8, v68
	v_mul_f32_e32 v3, v9, v69
	v_pk_mul_f32 v[4:5], v[12:13], v[72:73]
	v_pk_fma_f32 v[6:7], v[6:7], v[66:67], v[10:11]
	v_pk_fma_f32 v[8:9], v[8:9], v[68:69], v[4:5]
	v_pk_add_f32 v[92:93], v[6:7], v[92:93]
	v_cvt_pk_bf16_f32 v3, v2, v3
	v_pk_add_f32 v[90:91], v[8:9], v[32:33]
	v_cvt_pk_bf16_f32 v5, v4, v5
	v_cvt_pk_bf16_f32 v4, v10, v11
	ds_read_b128 v[26:29], v213 offset:36864
	ds_read_b128 v[6:9], v213 offset:16384
	v_cvt_pk_bf16_f32 v2, v30, v31
	ds_read_b128 v[98:101], v213 offset:25600
	ds_read_b128 v[102:105], v213 offset:37888
	v_mfma_f32_32x32x16_bf16 v[50:65], v[14:17], v[2:5], v[50:65]
	ds_read_b128 v[2:5], v213 offset:17408
	ds_read_b128 v[30:33], v213 offset:24576
	s_waitcnt lgkmcnt(4)
	v_pk_mul_f32 v[12:13], v[6:7], v[18:19]
	v_pk_mul_f32 v[10:11], v[8:9], v[20:21]
	s_waitcnt lgkmcnt(1)
	v_pk_mul_f32 v[14:15], v[2:3], v[22:23]
	v_pk_mul_f32 v[22:23], v[98:99], v[22:23]
	v_pk_fma_f32 v[112:113], v[6:7], v[18:19], v[14:15]
	s_waitcnt lgkmcnt(0)
	v_pk_mul_f32 v[114:115], v[30:31], v[18:19]
	v_pk_fma_f32 v[118:119], v[30:31], v[18:19], v[22:23]
	v_pk_mul_f32 v[4:5], v[4:5], v[24:25]
	v_pk_mul_f32 v[106:107], v[32:33], v[20:21]
	v_pk_mul_f32 v[24:25], v[100:101], v[24:25]
	ds_read_b128 v[98:101], v213 offset:18432
	v_cvt_pk_bf16_f32 v19, v106, v107
	ds_read_b128 v[106:109], v213 offset:19456
	v_pk_fma_f32 v[110:111], v[8:9], v[20:21], v[4:5]
	v_cvt_pk_bf16_f32 v5, v4, v5
	v_cvt_pk_bf16_f32 v3, v10, v11
	v_cvt_pk_bf16_f32 v4, v14, v15
	s_waitcnt lgkmcnt(0)
	v_pk_mul_f32 v[106:107], v[106:107], v[86:87]
	v_cvt_pk_bf16_f32 v2, v12, v13
	v_pk_mul_f32 v[120:121], v[98:99], v[82:83]
	v_pk_mul_f32 v[108:109], v[108:109], v[88:89]
	v_pk_fma_f32 v[98:99], v[98:99], v[82:83], v[106:107]
	v_mfma_f32_32x32x16_bf16 v[2:17], v[26:29], v[2:5], 0
	v_cvt_pk_bf16_f32 v18, v114, v115
	v_mul_f32_e32 v114, v100, v84
	v_mul_f32_e32 v115, v101, v85
	v_fma_f32 v100, v100, v84, v108
	v_fma_f32 v101, v101, v85, v109
	v_pk_add_f32 v[124:125], v[98:99], v[112:113]
	v_pk_add_f32 v[122:123], v[100:101], v[110:111]
	v_cvt_pk_bf16_f32 v101, v108, v109
	v_cvt_pk_bf16_f32 v100, v106, v107
	ds_read_b128 v[106:109], v213 offset:26624
	v_pk_fma_f32 v[116:117], v[32:33], v[20:21], v[24:25]
	v_cvt_pk_bf16_f32 v21, v24, v25
	v_cvt_pk_bf16_f32 v20, v22, v23
	ds_read_b128 v[110:113], v213 offset:27648
	v_cvt_pk_bf16_f32 v99, v114, v115
	v_mfma_f32_32x32x16_bf16 v[18:33], v[26:29], v[18:21], 0
	v_cvt_pk_bf16_f32 v98, v120, v121
	s_waitcnt lgkmcnt(1)
	v_mul_f32_e32 v114, v106, v82
	v_mul_f32_e32 v115, v107, v83
	s_waitcnt lgkmcnt(0)
	v_pk_mul_f32 v[86:87], v[110:111], v[86:87]
	v_pk_mul_f32 v[88:89], v[112:113], v[88:89]
	v_pk_fma_f32 v[82:83], v[106:107], v[82:83], v[86:87]
	v_mfma_f32_32x32x16_bf16 v[2:17], v[102:105], v[98:101], v[2:17]
	v_mul_f32_e32 v98, v108, v84
	v_mul_f32_e32 v99, v109, v85
	v_fma_f32 v84, v108, v84, v88
	v_fma_f32 v85, v109, v85, v89
	v_add_f32_e32 v108, v82, v118
	v_add_f32_e32 v109, v83, v119
	v_cvt_pk_bf16_f32 v83, v98, v99
	v_pk_add_f32 v[106:107], v[84:85], v[116:117]
	v_cvt_pk_bf16_f32 v85, v88, v89
	v_cvt_pk_bf16_f32 v84, v86, v87
	ds_read_b128 v[86:89], v213 offset:38912
	ds_read_b128 v[98:101], v213 offset:20480
	v_cvt_pk_bf16_f32 v82, v114, v115
	s_waitcnt lgkmcnt(0)
	v_pk_mul_f32 v[110:111], v[100:101], v[76:77]
	v_mfma_f32_32x32x16_bf16 v[18:33], v[102:105], v[82:85], v[18:33]
	ds_read_b128 v[82:85], v213 offset:21504
	ds_read_b128 v[102:105], v213 offset:28672
	v_mul_f32_e32 v112, v98, v74
	v_mul_f32_e32 v113, v99, v75
	s_waitcnt lgkmcnt(1)
	v_pk_mul_f32 v[84:85], v[84:85], v[80:81]
	v_pk_mul_f32 v[114:115], v[82:83], v[78:79]
	v_pk_fma_f32 v[82:83], v[100:101], v[76:77], v[84:85]
	v_cvt_pk_bf16_f32 v85, v84, v85
	v_pk_add_f32 v[116:117], v[82:83], v[122:123]
	v_cvt_pk_bf16_f32 v83, v110, v111
	v_cvt_pk_bf16_f32 v84, v114, v115
	v_cvt_pk_bf16_f32 v82, v112, v113
	v_pk_fma_f32 v[98:99], v[98:99], v[74:75], v[114:115]
	s_waitcnt lgkmcnt(0)
	v_pk_mul_f32 v[112:113], v[102:103], v[74:75]
	v_mfma_f32_32x32x16_bf16 v[2:17], v[86:89], v[82:85], v[2:17]
	ds_read_b128 v[82:85], v213 offset:29696
	v_add_f32_e32 v118, v98, v124
	v_add_f32_e32 v119, v99, v125
	v_mul_f32_e32 v110, v104, v76
	v_mul_f32_e32 v111, v105, v77
	ds_read_b128 v[98:101], v213 offset:39936
	s_waitcnt lgkmcnt(1)
	v_pk_mul_f32 v[78:79], v[82:83], v[78:79]
	v_pk_mul_f32 v[80:81], v[84:85], v[80:81]
	v_pk_fma_f32 v[74:75], v[102:103], v[74:75], v[78:79]
	v_pk_fma_f32 v[76:77], v[104:105], v[76:77], v[80:81]
	v_pk_add_f32 v[104:105], v[74:75], v[108:109]
	v_pk_add_f32 v[102:103], v[76:77], v[106:107]
	v_cvt_pk_bf16_f32 v77, v80, v81
	v_cvt_pk_bf16_f32 v76, v78, v79
	ds_read_b128 v[78:81], v213 offset:22528
	ds_read_b128 v[82:85], v213 offset:23552
	v_cvt_pk_bf16_f32 v75, v110, v111
	v_cvt_pk_bf16_f32 v74, v112, v113
	s_waitcnt lgkmcnt(0)
	v_pk_mul_f32 v[82:83], v[82:83], v[70:71]
	v_mfma_f32_32x32x16_bf16 v[18:33], v[86:89], v[74:77], v[18:33]
	v_mul_f32_e32 v74, v80, v68
	v_mul_f32_e32 v75, v81, v69
	v_mul_f32_e32 v76, v84, v72
	v_mul_f32_e32 v77, v85, v73
	v_mul_f32_e32 v86, v78, v66
	v_mul_f32_e32 v87, v79, v67
	v_pk_fma_f32 v[80:81], v[80:81], v[68:69], v[76:77]
	v_pk_fma_f32 v[78:79], v[78:79], v[66:67], v[82:83]
	v_cvt_pk_bf16_f32 v75, v74, v75
	v_pk_add_f32 v[88:89], v[80:81], v[116:117]
	v_pk_add_f32 v[106:107], v[78:79], v[118:119]
	ds_read_b128 v[78:81], v213 offset:30720
	v_cvt_pk_bf16_f32 v77, v76, v77
	v_cvt_pk_bf16_f32 v76, v82, v83
	ds_read_b128 v[82:85], v213 offset:31744
	v_cvt_pk_bf16_f32 v74, v86, v87
	s_waitcnt lgkmcnt(0)
	v_pk_mul_f32 v[72:73], v[84:85], v[72:73]
	v_mfma_f32_32x32x16_bf16 v[2:17], v[98:101], v[74:77], v[2:17]
	v_mul_f32_e32 v74, v80, v68
	v_mul_f32_e32 v75, v81, v69
	v_fma_f32 v68, v80, v68, v72
	v_fma_f32 v69, v81, v69, v73
	v_mul_f32_e32 v70, v82, v70
	v_mul_f32_e32 v71, v83, v71
	v_pk_add_f32 v[84:85], v[68:69], v[102:103]
	v_cvt_pk_bf16_f32 v69, v72, v73
	v_pk_mov_b32 v[72:73], v[96:97], v[94:95] op_sel:[1,0]
	v_mov_b32_e32 v97, v95
	v_pk_add_f32 v[72:73], v[72:73], v[96:97]
	v_pk_mul_f32 v[76:77], v[78:79], v[66:67]
	v_pk_fma_f32 v[66:67], v[78:79], v[66:67], v[70:71]
	v_pk_add_f32 v[72:73], v[72:73], v[72:73] op_sel:[0,1] op_sel_hi:[1,0]
	v_pk_add_f32 v[86:87], v[66:67], v[104:105]
	v_mov_b32_e32 v66, v72
	s_nop 1
	v_permlane32_swap_b32_e32 v72, v66
	v_add_f32_e32 v66, v72, v66
	v_cvt_pk_bf16_f32 v67, v74, v75
	v_rcp_f32_e32 v74, v66
	v_cvt_pk_bf16_f32 v68, v70, v71
	v_cvt_pk_bf16_f32 v66, v76, v77
	v_pk_mul_f32 v[70:71], v[46:47], v[74:75] op_sel_hi:[1,0]
	s_nop 0
	v_mfma_f32_32x32x16_bf16 v[18:33], v[98:101], v[66:69], v[18:33]
	v_mul_f32_e32 v66, v42, v74
	v_mul_f32_e32 v67, v43, v74
	v_pk_mov_b32 v[42:43], v[92:93], v[90:91] op_sel:[1,0]
	v_mov_b32_e32 v93, v91
	v_pk_add_f32 v[42:43], v[42:43], v[92:93]
	v_pk_mul_f32 v[68:69], v[44:45], v[74:75] op_sel_hi:[1,0]
	v_pk_add_f32 v[42:43], v[42:43], v[42:43] op_sel:[0,1] op_sel_hi:[1,0]
	v_pk_mov_b32 v[44:45], v[106:107], v[88:89] op_sel:[1,0]
	v_mov_b32_e32 v43, v42
	s_nop 1
	v_permlane32_swap_b32_e32 v42, v43
	v_add_f32_e32 v42, v42, v43
	v_rcp_f32_e32 v42, v42
	v_mov_b32_e32 v107, v89
	v_pk_add_f32 v[44:45], v[44:45], v[106:107]
	v_pk_mul_f32 v[72:73], v[48:49], v[74:75] op_sel_hi:[1,0]
	v_pk_add_f32 v[44:45], v[44:45], v[44:45] op_sel:[0,1] op_sel_hi:[1,0]
	v_pk_mul_f32 v[36:37], v[36:37], v[74:75] op_sel_hi:[1,0]
	v_pk_mul_f32 v[38:39], v[38:39], v[74:75] op_sel_hi:[1,0]
	v_pk_mul_f32 v[40:41], v[40:41], v[74:75] op_sel_hi:[1,0]
	v_pk_mul_f32 v[34:35], v[34:35], v[74:75] op_sel_hi:[1,0]
	v_pk_mul_f32 v[74:75], v[58:59], v[42:43] op_sel_hi:[1,0]
	v_pk_mul_f32 v[78:79], v[60:61], v[42:43] op_sel_hi:[1,0]
	v_pk_mul_f32 v[80:81], v[62:63], v[42:43] op_sel_hi:[1,0]
	v_pk_mul_f32 v[82:83], v[64:65], v[42:43] op_sel_hi:[1,0]
	v_pk_mul_f32 v[92:93], v[52:53], v[42:43] op_sel_hi:[1,0]
	v_mov_b32_e32 v43, v44
	s_nop 1
	v_permlane32_swap_b32_e32 v44, v43
	v_add_f32_e32 v43, v44, v43
	v_rcp_f32_e32 v76, v43
	v_pk_mul_f32 v[96:97], v[54:55], v[42:43] op_sel_hi:[1,0]
	v_pk_mul_f32 v[94:95], v[56:57], v[42:43] op_sel_hi:[1,0]
	v_pk_mul_f32 v[98:99], v[50:51], v[42:43] op_sel_hi:[1,0]
	v_pk_mul_f32 v[100:101], v[4:5], v[76:77] op_sel_hi:[1,0]
	v_pk_mov_b32 v[4:5], v[86:87], v[84:85] op_sel:[1,0]
	v_mov_b32_e32 v87, v85
	v_pk_add_f32 v[4:5], v[4:5], v[86:87]
	v_pk_mul_f32 v[102:103], v[6:7], v[76:77] op_sel_hi:[1,0]
	v_pk_add_f32 v[104:105], v[4:5], v[4:5] op_sel:[0,1] op_sel_hi:[1,0]
	v_cvt_pk_bf16_f32 v7, v40, v41
	ds_read_b128 v[84:87], v150 offset:52224
	ds_read_b128 v[50:53], v150 offset:35840
	ds_read_b128 v[54:57], v150 offset:36864
	ds_read_b128 v[58:61], v150 offset:37888
	ds_read_b128 v[62:65], v150 offset:38912
	v_cvt_pk_bf16_f32 v6, v38, v39
	v_cvt_pk_bf16_f32 v5, v36, v37
	v_cvt_pk_bf16_f32 v4, v34, v35
	ds_read_b128 v[88:91], v150 offset:53248
	ds_read_b128 v[34:37], v150 offset:39936
	ds_read_b128 v[38:41], v150 offset:40960
	ds_read_b128 v[42:45], v150 offset:41984
	ds_read_b128 v[46:49], v150 offset:43008
	v_cvt_pk_bf16_f32 v95, v94, v95
	v_cvt_pk_bf16_f32 v94, v96, v97
	v_cvt_pk_bf16_f32 v93, v92, v93
	v_cvt_pk_bf16_f32 v92, v98, v99
	s_waitcnt lgkmcnt(5)
	v_mfma_f32_32x32x16_bf16 v[50:65], v[84:87], v[4:7], v[50:65]
	v_mul_f32_e32 v10, v10, v76
	v_mul_f32_e32 v11, v11, v76
	v_mul_f32_e32 v12, v12, v76
	v_mul_f32_e32 v13, v13, v76
	v_mul_f32_e32 v8, v8, v76
	v_mul_f32_e32 v9, v9, v76
	v_mov_b32_e32 v77, v104
	s_nop 1
	v_permlane32_swap_b32_e32 v104, v77
	v_cvt_pk_bf16_f32 v73, v72, v73
	s_waitcnt lgkmcnt(0)
	v_mfma_f32_32x32x16_bf16 v[34:49], v[84:87], v[92:95], v[34:49]
	v_cvt_pk_bf16_f32 v72, v70, v71
	v_cvt_pk_bf16_f32 v70, v66, v67
	v_add_f32_e32 v66, v104, v77
	v_cvt_pk_bf16_f32 v71, v68, v69
	v_rcp_f32_e32 v104, v66
	v_cvt_pk_bf16_f32 v69, v82, v83
	v_cvt_pk_bf16_f32 v68, v80, v81
	v_cvt_pk_bf16_f32 v67, v78, v79
	v_cvt_pk_bf16_f32 v66, v74, v75
	ds_read_b128 v[78:81], v150 offset:54272
	v_mfma_f32_32x32x16_bf16 v[50:65], v[88:91], v[70:73], v[50:65]
	v_mul_f32_e32 v2, v2, v76
	v_mul_f32_e32 v3, v3, v76
	v_mul_f32_e32 v20, v20, v104
	v_mul_f32_e32 v21, v21, v104
	v_cvt_pk_bf16_f32 v85, v8, v9
	v_cvt_pk_bf16_f32 v82, v2, v3
	v_pk_mul_f32 v[2:3], v[22:23], v[104:105] op_sel_hi:[1,0]
	v_pk_mul_f32 v[8:9], v[24:25], v[104:105] op_sel_hi:[1,0]
	v_pk_mul_f32 v[18:19], v[18:19], v[104:105] op_sel_hi:[1,0]
	v_mfma_f32_32x32x16_bf16 v[34:49], v[88:91], v[66:69], v[34:49]
	v_cvt_pk_bf16_f32 v84, v102, v103
	v_cvt_pk_bf16_f32 v83, v100, v101
	ds_read_b128 v[86:89], v150 offset:55296
	v_cvt_pk_bf16_f32 v99, v8, v9
	v_cvt_pk_bf16_f32 v98, v2, v3
	v_cvt_pk_bf16_f32 v97, v20, v21
	v_cvt_pk_bf16_f32 v96, v18, v19
	s_waitcnt lgkmcnt(1)
	v_mfma_f32_32x32x16_bf16 v[50:65], v[78:81], v[82:85], v[50:65]
	v_mul_f32_e32 v2, v14, v76
	v_mul_f32_e32 v3, v15, v76
	v_mul_f32_e32 v8, v16, v76
	v_mul_f32_e32 v9, v17, v76
	v_mul_f32_e32 v14, v26, v104
	v_mul_f32_e32 v15, v27, v104
	v_cvt_pk_bf16_f32 v77, v8, v9
	v_cvt_pk_bf16_f32 v76, v2, v3
	v_cvt_pk_bf16_f32 v74, v10, v11
	v_pk_mul_f32 v[2:3], v[28:29], v[104:105] op_sel_hi:[1,0]
	v_mfma_f32_32x32x16_bf16 v[34:49], v[78:81], v[96:99], v[34:49]
	v_mul_f32_e32 v8, v30, v104
	v_mul_f32_e32 v9, v31, v104
	v_mul_f32_e32 v10, v32, v104
	v_mul_f32_e32 v11, v33, v104
	v_cvt_pk_bf16_f32 v75, v12, v13
	v_cvt_pk_bf16_f32 v81, v10, v11
	v_cvt_pk_bf16_f32 v80, v8, v9
	v_cvt_pk_bf16_f32 v79, v2, v3
	v_cvt_pk_bf16_f32 v78, v14, v15
	s_waitcnt lgkmcnt(0)
	v_mfma_f32_32x32x16_bf16 v[50:65], v[86:89], v[74:77], v[50:65]
	v_mfma_f32_32x32x16_bf16 v[34:49], v[86:89], v[78:81], v[34:49]
	ds_read_b128 v[86:89], v150 offset:56320
	ds_read_b128 v[18:21], v150 offset:44032
	ds_read_b128 v[22:25], v150 offset:45056
	ds_read_b128 v[26:29], v150 offset:46080
	ds_read_b128 v[30:33], v150 offset:47104
	ds_read_b128 v[100:103], v150 offset:57344
	s_waitcnt lgkmcnt(1)
	v_mfma_f32_32x32x16_bf16 v[18:33], v[86:89], v[4:7], v[18:33]
	ds_read_b128 v[2:5], v150 offset:48128
	ds_read_b128 v[6:9], v150 offset:49152
	ds_read_b128 v[10:13], v150 offset:50176
	ds_read_b128 v[14:17], v150 offset:51200
	s_waitcnt lgkmcnt(0)
	v_mfma_f32_32x32x16_bf16 v[2:17], v[86:89], v[92:95], v[2:17]
	v_mfma_f32_32x32x16_bf16 v[18:33], v[100:103], v[70:73], v[18:33]
	v_mfma_f32_32x32x16_bf16 v[2:17], v[100:103], v[66:69], v[2:17]
	ds_read_b128 v[66:69], v150 offset:58368
	ds_read_b128 v[70:73], v150 offset:59392
	s_waitcnt lgkmcnt(1)
	v_mfma_f32_32x32x16_bf16 v[18:33], v[66:69], v[82:85], v[18:33]
	v_mfma_f32_32x32x16_bf16 v[2:17], v[66:69], v[96:99], v[2:17]
	s_waitcnt lgkmcnt(0)
	v_mfma_f32_32x32x16_bf16 v[18:33], v[70:73], v[74:77], v[18:33]
	v_mfma_f32_32x32x16_bf16 v[2:17], v[70:73], v[78:81], v[2:17]
	s_nop 10
	v_mul_f32_e32 v66, v22, v22
	v_mul_f32_e32 v67, v23, v23
	v_mul_f32_e32 v68, v30, v30
	v_mul_f32_e32 v69, v31, v31
	v_mul_f32_e32 v70, v24, v24
	v_mul_f32_e32 v71, v25, v25
	v_pk_mul_f32 v[72:73], v[32:33], v[32:33]
	v_pk_mul_f32 v[74:75], v[20:21], v[20:21]
	v_pk_mul_f32 v[76:77], v[28:29], v[28:29]
	v_pk_mul_f32 v[78:79], v[26:27], v[26:27]
	v_pk_mul_f32 v[80:81], v[18:19], v[18:19]
	v_pk_fma_f32 v[78:79], v[58:59], v[58:59], v[78:79]
	v_pk_fma_f32 v[76:77], v[60:61], v[60:61], v[76:77]
	v_pk_fma_f32 v[74:75], v[52:53], v[52:53], v[74:75]
	v_pk_fma_f32 v[72:73], v[64:65], v[64:65], v[72:73]
	v_pk_fma_f32 v[70:71], v[56:57], v[56:57], v[70:71]
	v_pk_fma_f32 v[68:69], v[62:63], v[62:63], v[68:69]
	v_pk_fma_f32 v[66:67], v[54:55], v[54:55], v[66:67]
	v_pk_fma_f32 v[80:81], v[50:51], v[50:51], v[80:81]
	v_pk_add_f32 v[66:67], v[66:67], v[68:69]
	v_pk_add_f32 v[68:69], v[70:71], v[72:73]
	v_pk_add_f32 v[70:71], v[74:75], v[76:77]
	v_pk_add_f32 v[72:73], v[80:81], v[78:79]
	v_pk_add_f32 v[68:69], v[70:71], v[68:69]
	v_pk_add_f32 v[66:67], v[72:73], v[66:67]
	v_pk_mul_f32 v[72:73], v[14:15], v[14:15]
	v_pk_mov_b32 v[70:71], v[66:67], v[68:69] op_sel:[1,0]
	v_mov_b32_e32 v67, v69
	v_pk_add_f32 v[66:67], v[70:71], v[66:67]
	v_pk_mul_f32 v[70:71], v[6:7], v[6:7]
	v_pk_mul_f32 v[74:75], v[8:9], v[8:9]
	v_pk_mul_f32 v[76:77], v[16:17], v[16:17]
	v_pk_mul_f32 v[78:79], v[4:5], v[4:5]
	v_pk_mul_f32 v[80:81], v[12:13], v[12:13]
	v_pk_mul_f32 v[82:83], v[10:11], v[10:11]
	v_pk_mul_f32 v[84:85], v[2:3], v[2:3]
	v_pk_fma_f32 v[82:83], v[42:43], v[42:43], v[82:83]
	v_pk_fma_f32 v[80:81], v[44:45], v[44:45], v[80:81]
	v_pk_fma_f32 v[78:79], v[36:37], v[36:37], v[78:79]
	v_pk_fma_f32 v[76:77], v[48:49], v[48:49], v[76:77]
	v_pk_fma_f32 v[74:75], v[40:41], v[40:41], v[74:75]
	v_pk_fma_f32 v[72:73], v[46:47], v[46:47], v[72:73]
	v_pk_fma_f32 v[70:71], v[38:39], v[38:39], v[70:71]
	v_pk_fma_f32 v[84:85], v[34:35], v[34:35], v[84:85]
	v_pk_add_f32 v[70:71], v[70:71], v[72:73]
	v_pk_add_f32 v[72:73], v[74:75], v[76:77]
	v_pk_add_f32 v[74:75], v[78:79], v[80:81]
	v_pk_add_f32 v[76:77], v[84:85], v[82:83]
	v_pk_add_f32 v[72:73], v[74:75], v[72:73]
	v_pk_add_f32 v[70:71], v[76:77], v[70:71]
	v_pk_add_f32 v[66:67], v[66:67], v[66:67] op_sel:[0,1] op_sel_hi:[1,0]
	v_pk_mov_b32 v[74:75], v[70:71], v[72:73] op_sel:[1,0]
	v_mov_b32_e32 v71, v73
	v_pk_add_f32 v[70:71], v[74:75], v[70:71]
	v_mov_b32_e32 v69, v66
	v_pk_add_f32 v[70:71], v[70:71], v[70:71] op_sel:[0,1] op_sel_hi:[1,0]
	s_nop 0
	v_permlane32_swap_b32_e32 v66, v69
	v_mov_b32_e32 v68, v70
	s_nop 1
	v_permlane32_swap_b32_e32 v70, v68
	v_mov_b32_e32 v71, v66
	v_pk_add_f32 v[66:67], v[70:71], v[68:69]
	v_pk_fma_f32 v[66:67], v[66:67], s[0:1], v[152:153] op_sel_hi:[1,0,0]
	s_mov_b32 s1, 0x800000
	v_mul_f32_e32 v68, 0x4b800000, v67
	v_cmp_gt_f32_e32 vcc, s1, v67
	s_nop 1
	v_cndmask_b32_e32 v67, v67, v68, vcc
	v_rsq_f32_e32 v67, v67
	s_nop 0
	v_mul_f32_e32 v68, 0x45800000, v67
	v_cndmask_b32_e32 v68, v67, v68, vcc
	v_pk_mul_f32 v[158:159], v[50:51], v[68:69] op_sel_hi:[1,0]
	v_pk_mul_f32 v[50:51], v[18:19], v[68:69] op_sel_hi:[1,0]
	v_mul_f32_e32 v18, 0x4b800000, v66
	v_cmp_gt_f32_e32 vcc, s1, v66
	v_pk_mul_f32 v[80:81], v[60:61], v[68:69] op_sel_hi:[1,0]
	v_pk_mul_f32 v[60:61], v[28:29], v[68:69] op_sel_hi:[1,0]
	v_cndmask_b32_e32 v18, v66, v18, vcc
	v_rsq_f32_e32 v18, v18
	v_pk_mul_f32 v[78:79], v[58:59], v[68:69] op_sel_hi:[1,0]
	v_pk_mul_f32 v[160:161], v[52:53], v[68:69] op_sel_hi:[1,0]
	v_pk_mul_f32 v[82:83], v[54:55], v[68:69] op_sel_hi:[1,0]
	v_mul_f32_e32 v19, 0x45800000, v18
	v_cndmask_b32_e32 v28, v18, v19, vcc
	v_pk_mul_f32 v[168:169], v[56:57], v[68:69] op_sel_hi:[1,0]
	v_pk_mul_f32 v[58:59], v[26:27], v[68:69] op_sel_hi:[1,0]
	v_pk_mul_f32 v[52:53], v[20:21], v[68:69] op_sel_hi:[1,0]
	v_pk_mul_f32 v[54:55], v[22:23], v[68:69] op_sel_hi:[1,0]
	v_pk_mul_f32 v[56:57], v[24:25], v[68:69] op_sel_hi:[1,0]
	v_pk_mul_f32 v[18:19], v[42:43], v[28:29] op_sel_hi:[1,0]
	v_pk_mul_f32 v[20:21], v[44:45], v[28:29] op_sel_hi:[1,0]
	v_pk_mul_f32 v[22:23], v[46:47], v[28:29] op_sel_hi:[1,0]
	v_pk_mul_f32 v[26:27], v[48:49], v[28:29] op_sel_hi:[1,0]
	v_pk_mul_f32 v[162:163], v[34:35], v[28:29] op_sel_hi:[1,0]
	v_pk_mul_f32 v[164:165], v[36:37], v[28:29] op_sel_hi:[1,0]
	v_pk_mul_f32 v[166:167], v[38:39], v[28:29] op_sel_hi:[1,0]
	v_pk_mul_f32 v[24:25], v[40:41], v[28:29] op_sel_hi:[1,0]
	v_pk_mul_f32 v[104:105], v[2:3], v[28:29] op_sel_hi:[1,0]
	v_pk_mul_f32 v[112:113], v[4:5], v[28:29] op_sel_hi:[1,0]
	s_nop 0
	s_nop 0
	ds_read_b128 v[2:5], v150 offset:60416
	ds_read_b128 v[34:37], v174 offset:32768
	ds_read_b128 v[38:41], v174 offset:32800
	ds_read_b128 v[42:45], v174 offset:32832
	ds_read_b128 v[46:49], v174 offset:32864
	v_cvt_pk_bf16_f32 v129, v168, v169
	v_cvt_pk_bf16_f32 v128, v82, v83
	v_cvt_pk_bf16_f32 v127, v160, v161
	v_cvt_pk_bf16_f32 v126, v158, v159
	v_cvt_pk_bf16_f32 v137, v24, v25
	v_cvt_pk_bf16_f32 v136, v166, v167
	v_cvt_pk_bf16_f32 v135, v164, v165
	s_waitcnt lgkmcnt(0)
	v_mfma_f32_32x32x16_bf16 v[86:101], v[2:5], v[126:129], v[34:49]
	v_cvt_pk_bf16_f32 v134, v162, v163
	v_mul_f32_e32 v84, v62, v68
	v_mul_f32_e32 v85, v63, v68
	v_mul_f32_e32 v170, v64, v68
	v_mul_f32_e32 v171, v65, v68
	v_pk_mul_f32 v[62:63], v[30:31], v[68:69] op_sel_hi:[1,0]
	v_pk_mul_f32 v[64:65], v[32:33], v[68:69] op_sel_hi:[1,0]
	v_pk_mul_f32 v[116:117], v[6:7], v[28:29] op_sel_hi:[1,0]
	v_pk_mul_f32 v[154:155], v[8:9], v[28:29] op_sel_hi:[1,0]
	v_mfma_f32_32x32x16_bf16 v[34:49], v[2:5], v[134:137], v[34:49]
	ds_read_b128 v[6:9], v150 offset:61440
	ds_read_b128 v[66:69], v174 offset:32896
	ds_read_b128 v[106:109], v150 offset:64512
	v_cvt_pk_bf16_f32 v125, v170, v171
	v_cvt_pk_bf16_f32 v124, v84, v85
	v_cvt_pk_bf16_f32 v123, v80, v81
	v_cvt_pk_bf16_f32 v122, v78, v79
	v_cvt_pk_bf16_f32 v149, v26, v27
	v_cvt_pk_bf16_f32 v148, v22, v23
	v_cvt_pk_bf16_f32 v147, v20, v21
	v_cvt_pk_bf16_f32 v146, v18, v19
	s_waitcnt lgkmcnt(2)
	v_mfma_f32_32x32x16_bf16 v[86:101], v[6:9], v[122:125], v[86:101]
	v_mul_f32_e32 v102, v10, v28
	v_mul_f32_e32 v103, v11, v28
	v_mul_f32_e32 v110, v12, v28
	v_mul_f32_e32 v111, v13, v28
	v_mul_f32_e32 v114, v14, v28
	v_mul_f32_e32 v115, v15, v28
	v_pk_mul_f32 v[156:157], v[16:17], v[28:29] op_sel_hi:[1,0]
	ds_read_b128 v[176:179], v174 offset:33536
	ds_read_b128 v[180:183], v174 offset:33568
	ds_read_b128 v[184:187], v174 offset:33600
	ds_read_b128 v[28:31], v174 offset:33632
	ds_read_b128 v[188:191], v174 offset:33792
	ds_read_b128 v[192:195], v174 offset:33824
	ds_read_b128 v[196:199], v174 offset:33856
	ds_read_b128 v[200:203], v174 offset:33888
	ds_read_b128 v[204:207], v150 offset:62464
	v_cvt_pk_bf16_f32 v133, v56, v57
	v_mfma_f32_32x32x16_bf16 v[34:49], v[6:9], v[146:149], v[34:49]
	v_cvt_pk_bf16_f32 v132, v54, v55
	v_cvt_pk_bf16_f32 v131, v52, v53
	v_cvt_pk_bf16_f32 v130, v50, v51
	ds_read_b128 v[70:73], v174 offset:33664
	ds_read_b128 v[74:77], v174 offset:33920
	ds_read_b128 v[208:211], v150 offset:63488
	v_cvt_pk_bf16_f32 v145, v154, v155
	v_cvt_pk_bf16_f32 v144, v116, v117
	v_cvt_pk_bf16_f32 v143, v112, v113
	v_cvt_pk_bf16_f32 v142, v104, v105
	s_waitcnt lgkmcnt(3)
	v_mfma_f32_32x32x16_bf16 v[86:101], v[204:207], v[130:133], v[86:101]
	v_cvt_pk_bf16_f32 v121, v64, v65
	v_cvt_pk_bf16_f32 v120, v62, v63
	v_cvt_pk_bf16_f32 v119, v60, v61
	v_cvt_pk_bf16_f32 v118, v58, v59
	v_cvt_pk_bf16_f32 v141, v156, v157
	v_cvt_pk_bf16_f32 v140, v114, v115
	v_cvt_pk_bf16_f32 v139, v110, v111
	v_mfma_f32_32x32x16_bf16 v[34:49], v[204:207], v[142:145], v[34:49]
	v_cvt_pk_bf16_f32 v138, v102, v103
	v_fma_f32 v16, v30, v170, v202
	v_fma_f32 v17, v31, v171, v203
	v_fma_f32 v14, v28, v84, v200
	v_fma_f32 v15, v29, v85, v201
	v_pk_fma_f32 v[12:13], v[186:187], v[80:81], v[198:199]
	v_pk_fma_f32 v[10:11], v[184:185], v[78:79], v[196:197]
	v_pk_fma_f32 v[8:9], v[182:183], v[168:169], v[194:195]
	s_waitcnt lgkmcnt(0)
	v_mfma_f32_32x32x16_bf16 v[86:101], v[208:211], v[118:121], v[86:101]
	v_fma_f32 v6, v180, v82, v192
	v_fma_f32 v7, v181, v83, v193
	ds_read_b128 v[78:81], v174 offset:33760
	ds_read_b128 v[82:85], v174 offset:33248
	v_fma_f32 v4, v178, v160, v190
	v_fma_f32 v5, v179, v161, v191
	v_pk_fma_f32 v[2:3], v[176:177], v[158:159], v[188:189]
	v_pk_fma_f32 v[32:33], v[30:31], v[26:27], v[202:203]
	v_pk_fma_f32 v[30:31], v[28:29], v[22:23], v[200:201]
	v_pk_fma_f32 v[28:29], v[186:187], v[20:21], v[198:199]
	v_pk_fma_f32 v[26:27], v[184:185], v[18:19], v[196:197]
	v_pk_fma_f32 v[24:25], v[182:183], v[24:25], v[194:195]
	v_pk_fma_f32 v[22:23], v[180:181], v[166:167], v[192:193]
	v_pk_fma_f32 v[20:21], v[178:179], v[164:165], v[190:191]
	v_pk_fma_f32 v[18:19], v[176:177], v[162:163], v[188:189]
	ds_read_b128 v[158:161], v174 offset:33696
	ds_read_b128 v[162:165], v174 offset:33728
	ds_read_b128 v[166:169], v174 offset:33952
	ds_read_b128 v[176:179], v174 offset:33984
	ds_read_b128 v[180:183], v174 offset:34016
	ds_read_b128 v[184:187], v212 offset:11264
	v_mfma_f32_32x32x16_bf16 v[34:49], v[208:211], v[138:141], v[34:49]
	v_cvt_pk_bf16_f32 v86, v86, v87
	v_cvt_pk_bf16_f32 v87, v88, v89
	v_cvt_pk_bf16_f32 v88, v90, v91
	v_cvt_pk_bf16_f32 v89, v92, v93
	ds_read_b128 v[90:93], v212 offset:12288
	v_pk_max_i16 v86, v86, 0
	v_pk_max_i16 v87, v87, 0
	v_pk_max_i16 v88, v88, 0
	v_pk_max_i16 v89, v89, 0
	s_nop 1
	s_nop 0
	v_cvt_pk_bf16_f32 v188, v34, v35
	v_cvt_pk_bf16_f32 v189, v36, v37
	v_cvt_pk_bf16_f32 v190, v38, v39
	v_cvt_pk_bf16_f32 v191, v40, v41
	s_waitcnt lgkmcnt(1)
	v_mfma_f32_32x32x16_bf16 v[2:17], v[184:187], v[86:89], v[2:17]
	v_pk_max_i16 v188, v188, 0
	v_pk_max_i16 v189, v189, 0
	v_pk_max_i16 v190, v190, 0
	v_pk_max_i16 v191, v191, 0
	v_cvt_pk_bf16_f32 v94, v94, v95
	v_cvt_pk_bf16_f32 v95, v96, v97
	v_cvt_pk_bf16_f32 v96, v98, v99
	v_cvt_pk_bf16_f32 v97, v100, v101
	v_cvt_pk_bf16_f32 v98, v42, v43
	v_cvt_pk_bf16_f32 v99, v44, v45
	v_mfma_f32_32x32x16_bf16 v[18:33], v[184:187], v[188:191], v[18:33]
	ds_read_b128 v[184:187], v212 offset:19456
	v_cvt_pk_bf16_f32 v100, v46, v47
	v_cvt_pk_bf16_f32 v101, v48, v49
	v_fma_f32 v64, v80, v64, v182
	v_fma_f32 v65, v81, v65, v183
	v_pk_fma_f32 v[62:63], v[78:79], v[62:63], v[180:181]
	v_pk_fma_f32 v[60:61], v[164:165], v[60:61], v[178:179]
	v_pk_fma_f32 v[58:59], v[162:163], v[58:59], v[176:177]
	v_pk_max_i16 v94, v94, 0
	v_pk_max_i16 v95, v95, 0
	v_pk_max_i16 v96, v96, 0
	v_pk_max_i16 v97, v97, 0
	v_pk_max_i16 v98, v98, 0
	v_pk_max_i16 v99, v99, 0
	v_pk_max_i16 v100, v100, 0
	v_pk_max_i16 v101, v101, 0
	v_pk_fma_f32 v[56:57], v[160:161], v[56:57], v[168:169]
	s_waitcnt lgkmcnt(1)
	v_mfma_f32_32x32x16_bf16 v[2:17], v[90:93], v[94:97], v[2:17]
	v_fma_f32 v54, v158, v54, v166
	v_fma_f32 v55, v159, v55, v167
	v_fma_f32 v52, v72, v52, v76
	v_fma_f32 v53, v73, v53, v77
	v_fma_f32 v50, v70, v50, v74
	v_fma_f32 v51, v71, v51, v75
	v_pk_fma_f32 v[48:49], v[80:81], v[156:157], v[182:183]
	v_pk_fma_f32 v[46:47], v[78:79], v[114:115], v[180:181]
	v_pk_fma_f32 v[44:45], v[164:165], v[110:111], v[178:179]
	v_pk_fma_f32 v[42:43], v[162:163], v[102:103], v[176:177]
	v_mfma_f32_32x32x16_bf16 v[18:33], v[90:93], v[98:101], v[18:33]
	ds_read_b128 v[90:93], v212 offset:20480
	v_fma_f32 v40, v160, v154, v168
	v_fma_f32 v41, v161, v155, v169
	v_fma_f32 v38, v158, v116, v166
	v_fma_f32 v39, v159, v117, v167
	v_pk_fma_f32 v[36:37], v[72:73], v[112:113], v[76:77]
	v_pk_fma_f32 v[34:35], v[70:71], v[104:105], v[74:75]
	s_waitcnt lgkmcnt(1)
	v_mfma_f32_32x32x16_bf16 v[50:65], v[184:187], v[86:89], v[50:65]
	ds_read_b128 v[70:73], v174 offset:32928
	ds_read_b128 v[74:77], v174 offset:32960
	ds_read_b128 v[78:81], v174 offset:32992
	ds_read_b128 v[86:89], v174 offset:33024
	ds_read_b128 v[110:113], v212 offset:1024
	v_mfma_f32_32x32x16_bf16 v[34:49], v[184:187], v[188:191], v[34:49]
	s_waitcnt lgkmcnt(5)
	v_mfma_f32_32x32x16_bf16 v[50:65], v[90:93], v[94:97], v[50:65]
	v_mfma_f32_32x32x16_bf16 v[34:49], v[90:93], v[98:101], v[34:49]
	s_waitcnt lgkmcnt(2)
	v_mfma_f32_32x32x16_bf16 v[90:105], v[106:109], v[126:129], v[66:81]
	v_mfma_f32_32x32x16_bf16 v[66:81], v[106:109], v[134:137], v[66:81]
	ds_read_b128 v[106:109], v212 offset:0
	s_waitcnt lgkmcnt(0)
	v_mfma_f32_32x32x16_bf16 v[90:105], v[106:109], v[122:125], v[90:105]
	v_mfma_f32_32x32x16_bf16 v[66:81], v[106:109], v[146:149], v[66:81]
	ds_read_b128 v[106:109], v212 offset:2048
	v_mfma_f32_32x32x16_bf16 v[90:105], v[110:113], v[130:133], v[90:105]
	v_mfma_f32_32x32x16_bf16 v[66:81], v[110:113], v[142:145], v[66:81]
	ds_read_b128 v[110:113], v212 offset:13312
	s_waitcnt lgkmcnt(1)
	v_mfma_f32_32x32x16_bf16 v[90:105], v[106:109], v[118:121], v[90:105]
	v_mfma_f32_32x32x16_bf16 v[66:81], v[106:109], v[138:141], v[66:81]
	s_nop 10
	v_cvt_pk_bf16_f32 v90, v90, v91
	v_cvt_pk_bf16_f32 v91, v92, v93
	v_cvt_pk_bf16_f32 v92, v94, v95
	v_cvt_pk_bf16_f32 v94, v98, v99
	v_cvt_pk_bf16_f32 v95, v100, v101
	ds_read_b128 v[98:101], v212 offset:21504
	v_cvt_pk_bf16_f32 v66, v66, v67
	v_cvt_pk_bf16_f32 v67, v68, v69
	v_cvt_pk_bf16_f32 v68, v70, v71
	v_cvt_pk_bf16_f32 v93, v96, v97
	v_cvt_pk_bf16_f32 v69, v72, v73
	ds_read_b128 v[70:73], v212 offset:14336
	v_pk_max_i16 v90, v90, 0
	v_pk_max_i16 v91, v91, 0
	v_pk_max_i16 v92, v92, 0
	v_pk_max_i16 v93, v93, 0
	v_pk_max_i16 v66, v66, 0
	v_pk_max_i16 v67, v67, 0
	v_pk_max_i16 v68, v68, 0
	v_pk_max_i16 v69, v69, 0
	v_cvt_pk_bf16_f32 v96, v102, v103
	s_waitcnt lgkmcnt(2)
	v_mfma_f32_32x32x16_bf16 v[2:17], v[110:113], v[90:93], v[2:17]
	v_cvt_pk_bf16_f32 v97, v104, v105
	v_cvt_pk_bf16_f32 v74, v74, v75
	v_cvt_pk_bf16_f32 v75, v76, v77
	v_cvt_pk_bf16_f32 v76, v78, v79
	v_cvt_pk_bf16_f32 v77, v80, v81
	v_pk_max_i16 v94, v94, 0
	v_pk_max_i16 v95, v95, 0
	v_pk_max_i16 v96, v96, 0
	v_pk_max_i16 v97, v97, 0
	v_pk_max_i16 v74, v74, 0
	v_pk_max_i16 v75, v75, 0
	v_pk_max_i16 v76, v76, 0
	v_pk_max_i16 v77, v77, 0
	v_mfma_f32_32x32x16_bf16 v[18:33], v[110:113], v[66:69], v[18:33]
	s_waitcnt lgkmcnt(1)
	v_mfma_f32_32x32x16_bf16 v[34:49], v[98:101], v[66:69], v[34:49]
	ds_read_b128 v[66:69], v212 offset:22528
	v_mfma_f32_32x32x16_bf16 v[50:65], v[98:101], v[90:93], v[50:65]
	s_waitcnt lgkmcnt(1)
	v_mfma_f32_32x32x16_bf16 v[2:17], v[70:73], v[94:97], v[2:17]
	v_mfma_f32_32x32x16_bf16 v[18:33], v[70:73], v[74:77], v[18:33]
	ds_read_b128 v[78:81], v212 offset:3072
	s_waitcnt lgkmcnt(1)
	v_mfma_f32_32x32x16_bf16 v[50:65], v[66:69], v[94:97], v[50:65]
	ds_read_b128 v[90:93], v174 offset:33056
	ds_read_b128 v[94:97], v174 offset:33088
	ds_read_b128 v[98:101], v174 offset:33120
	ds_read_b128 v[70:73], v174 offset:33152
	v_mfma_f32_32x32x16_bf16 v[34:49], v[66:69], v[74:77], v[34:49]
	ds_read_b128 v[66:69], v212 offset:4096
	ds_read_b128 v[74:77], v212 offset:5120
	s_waitcnt lgkmcnt(3)
	v_mfma_f32_32x32x16_bf16 v[102:117], v[78:81], v[126:129], v[86:101]
	v_mfma_f32_32x32x16_bf16 v[86:101], v[78:81], v[134:137], v[86:101]
	s_waitcnt lgkmcnt(1)
	v_mfma_f32_32x32x16_bf16 v[86:101], v[66:69], v[146:149], v[86:101]
	v_mfma_f32_32x32x16_bf16 v[102:117], v[66:69], v[122:125], v[102:117]
	ds_read_b128 v[66:69], v212 offset:6144
	s_waitcnt lgkmcnt(1)
	v_mfma_f32_32x32x16_bf16 v[86:101], v[74:77], v[142:145], v[86:101]
	v_mfma_f32_32x32x16_bf16 v[102:117], v[74:77], v[130:133], v[102:117]
	ds_read_b128 v[74:77], v212 offset:15360
	s_waitcnt lgkmcnt(1)
	v_mfma_f32_32x32x16_bf16 v[86:101], v[66:69], v[138:141], v[86:101]
	v_mfma_f32_32x32x16_bf16 v[102:117], v[66:69], v[118:121], v[102:117]
	s_nop 10
	v_cvt_pk_bf16_f32 v78, v86, v87
	v_cvt_pk_bf16_f32 v80, v90, v91
	v_cvt_pk_bf16_f32 v79, v88, v89
	v_cvt_pk_bf16_f32 v81, v92, v93
	ds_read_b128 v[86:89], v212 offset:16384
	ds_read_b128 v[90:93], v212 offset:23552
	v_cvt_pk_bf16_f32 v66, v102, v103
	v_cvt_pk_bf16_f32 v67, v104, v105
	v_cvt_pk_bf16_f32 v68, v106, v107
	v_cvt_pk_bf16_f32 v69, v108, v109
	v_pk_max_i16 v66, v66, 0
	v_pk_max_i16 v67, v67, 0
	v_pk_max_i16 v68, v68, 0
	v_pk_max_i16 v69, v69, 0
	v_pk_max_i16 v78, v78, 0
	v_pk_max_i16 v79, v79, 0
	v_pk_max_i16 v80, v80, 0
	v_pk_max_i16 v81, v81, 0
	v_cvt_pk_bf16_f32 v94, v94, v95
	s_waitcnt lgkmcnt(2)
	v_mfma_f32_32x32x16_bf16 v[18:33], v[74:77], v[78:81], v[18:33]
	v_cvt_pk_bf16_f32 v95, v96, v97
	v_cvt_pk_bf16_f32 v96, v98, v99
	v_cvt_pk_bf16_f32 v97, v100, v101
	v_pk_max_i16 v94, v94, 0
	v_pk_max_i16 v95, v95, 0
	v_pk_max_i16 v96, v96, 0
	v_pk_max_i16 v97, v97, 0
	v_mfma_f32_32x32x16_bf16 v[2:17], v[74:77], v[66:69], v[2:17]
	v_cvt_pk_bf16_f32 v74, v110, v111
	v_cvt_pk_bf16_f32 v75, v112, v113
	v_cvt_pk_bf16_f32 v76, v114, v115
	v_cvt_pk_bf16_f32 v77, v116, v117
	v_pk_max_i16 v74, v74, 0
	v_pk_max_i16 v75, v75, 0
	v_pk_max_i16 v76, v76, 0
	v_pk_max_i16 v77, v77, 0
	s_waitcnt lgkmcnt(0)
	v_mfma_f32_32x32x16_bf16 v[50:65], v[90:93], v[66:69], v[50:65]
	ds_read_b128 v[66:69], v212 offset:24576
	v_mfma_f32_32x32x16_bf16 v[34:49], v[90:93], v[78:81], v[34:49]
	ds_read_b128 v[102:105], v212 offset:7168
	v_mfma_f32_32x32x16_bf16 v[2:17], v[86:89], v[74:77], v[2:17]
	s_waitcnt lgkmcnt(1)
	v_mfma_f32_32x32x16_bf16 v[50:65], v[66:69], v[74:77], v[50:65]
	ds_read_b128 v[74:77], v174 offset:33184
	ds_read_b128 v[78:81], v174 offset:33216
	v_mfma_f32_32x32x16_bf16 v[34:49], v[66:69], v[94:97], v[34:49]
	ds_read_b128 v[66:69], v212 offset:8192
	v_mfma_f32_32x32x16_bf16 v[18:33], v[86:89], v[94:97], v[18:33]
	s_waitcnt lgkmcnt(1)
	v_mfma_f32_32x32x16_bf16 v[86:101], v[102:105], v[126:129], v[70:85]
	v_mfma_f32_32x32x16_bf16 v[70:85], v[102:105], v[134:137], v[70:85]
	ds_read_b128 v[102:105], v212 offset:9216
	v_lshlrev_b32_e32 v135, 2, v1
	v_add_u32_e32 v134, v172, v174
	s_waitcnt lgkmcnt(1)
	v_mfma_f32_32x32x16_bf16 v[86:101], v[66:69], v[122:125], v[86:101]
	v_mfma_f32_32x32x16_bf16 v[70:85], v[66:69], v[146:149], v[70:85]
	ds_read_b128 v[66:69], v212 offset:10240
	s_waitcnt lgkmcnt(1)
	v_mfma_f32_32x32x16_bf16 v[86:101], v[102:105], v[130:133], v[86:101]
	v_mfma_f32_32x32x16_bf16 v[70:85], v[102:105], v[142:145], v[70:85]
	ds_read_b128 v[102:105], v212 offset:17408
	s_waitcnt lgkmcnt(1)
	v_mfma_f32_32x32x16_bf16 v[86:101], v[66:69], v[118:121], v[86:101]
	v_mfma_f32_32x32x16_bf16 v[70:85], v[66:69], v[138:141], v[70:85]
	s_nop 10
	v_cvt_pk_bf16_f32 v68, v90, v91
	v_cvt_pk_bf16_f32 v69, v92, v93
	ds_read_b128 v[90:93], v212 offset:25600
	v_cvt_pk_bf16_f32 v66, v86, v87
	v_cvt_pk_bf16_f32 v67, v88, v89
	v_pk_max_i16 v66, v66, 0
	v_pk_max_i16 v67, v67, 0
	v_pk_max_i16 v68, v68, 0
	v_pk_max_i16 v69, v69, 0
	v_cvt_pk_bf16_f32 v70, v70, v71
	v_cvt_pk_bf16_f32 v71, v72, v73
	s_waitcnt lgkmcnt(1)
	v_mfma_f32_32x32x16_bf16 v[2:17], v[102:105], v[66:69], v[2:17]
	v_cvt_pk_bf16_f32 v72, v74, v75
	v_cvt_pk_bf16_f32 v73, v76, v77
	ds_read_b128 v[74:77], v212 offset:18432
	v_cvt_pk_bf16_f32 v86, v94, v95
	v_cvt_pk_bf16_f32 v87, v96, v97
	v_cvt_pk_bf16_f32 v88, v98, v99
	s_waitcnt lgkmcnt(1)
	v_mfma_f32_32x32x16_bf16 v[50:65], v[90:93], v[66:69], v[50:65]
	ds_read_b128 v[66:69], v212 offset:26624
	v_cvt_pk_bf16_f32 v89, v100, v101
	v_pk_max_i16 v86, v86, 0
	v_pk_max_i16 v87, v87, 0
	v_pk_max_i16 v88, v88, 0
	v_pk_max_i16 v89, v89, 0
	v_pk_max_i16 v70, v70, 0
	v_pk_max_i16 v71, v71, 0
	v_pk_max_i16 v72, v72, 0
	v_pk_max_i16 v73, v73, 0
	v_cvt_pk_bf16_f32 v78, v78, v79
	v_cvt_pk_bf16_f32 v79, v80, v81
	s_waitcnt lgkmcnt(1)
	v_mfma_f32_32x32x16_bf16 v[2:17], v[74:77], v[86:89], v[2:17]
	v_cvt_pk_bf16_f32 v80, v82, v83
	v_cvt_pk_bf16_f32 v81, v84, v85
	v_pk_max_i16 v78, v78, 0
	v_pk_max_i16 v79, v79, 0
	v_pk_max_i16 v80, v80, 0
	v_pk_max_i16 v81, v81, 0
	s_waitcnt lgkmcnt(0)
	v_mfma_f32_32x32x16_bf16 v[50:65], v[66:69], v[86:89], v[50:65]
	v_mfma_f32_32x32x16_bf16 v[34:49], v[90:93], v[70:73], v[34:49]
	s_nop 10
	v_add_f32_e32 v130, v10, v58
	v_add_f32_e32 v131, v11, v59
	v_add_f32_e32 v132, v12, v60
	v_add_f32_e32 v133, v13, v61
	v_add_f32_e32 v138, v4, v52
	v_add_f32_e32 v139, v5, v53
	v_pk_add_f32 v[140:141], v[16:17], v[64:65]
	v_pk_add_f32 v[142:143], v[8:9], v[56:57]
	v_pk_add_f32 v[144:145], v[14:15], v[62:63]
	v_pk_add_f32 v[146:147], v[6:7], v[54:55]
	v_mfma_f32_32x32x16_bf16 v[18:33], v[102:105], v[70:73], v[18:33]
	ds_read2st64_b32 v[70:71], v135 offset0:133 offset1:134
	v_add_f32_e32 v148, v2, v50
	v_add_f32_e32 v149, v3, v51
	v_add_f32_e32 v144, v146, v144
	v_add_f32_e32 v145, v147, v145
	v_pk_add_f32 v[140:141], v[142:143], v[140:141]
	v_pk_add_f32 v[132:133], v[138:139], v[132:133]
	v_pk_add_f32 v[130:131], v[148:149], v[130:131]
	v_pk_add_f32 v[132:133], v[132:133], v[140:141]
	v_pk_add_f32 v[130:131], v[130:131], v[144:145]
	v_mfma_f32_32x32x16_bf16 v[34:49], v[66:69], v[78:81], v[34:49]
	v_pk_mov_b32 v[138:139], v[130:131], v[132:133] op_sel:[1,0]
	v_mov_b32_e32 v131, v133
	s_waitcnt vmcnt(0) lgkmcnt(0)
	v_mul_f32_e32 v66, v175, v70
	v_pk_add_f32 v[130:131], v[138:139], v[130:131]
	ds_write_b32 v173, v66 offset:512
	v_mul_f32_e32 v66, v175, v71
	v_pk_add_f32 v[130:131], v[130:131], v[130:131] op_sel:[0,1] op_sel_hi:[1,0]
	s_waitcnt lgkmcnt(0)
	ds_read_b128 v[102:105], v174 offset:34560
	ds_read_b128 v[98:101], v174 offset:34592
	ds_read_b128 v[110:113], v174 offset:34624
	ds_read_b128 v[106:109], v174 offset:34656
	ds_read_b128 v[114:117], v174 offset:34688
	ds_read_b128 v[122:125], v174 offset:34720
	ds_read_b128 v[118:121], v174 offset:34752
	ds_read_b128 v[126:129], v174 offset:34784
	v_mov_b32_dpp v66, v66 quad_perm:[1,0,3,2] row_mask:0xf bank_mask:0xf bound_ctrl:1
	v_mov_b32_e32 v131, v130
	v_fmac_f32_e32 v66, v175, v71
	s_nop 0
	v_permlane32_swap_b32_e32 v130, v131
	v_add_f32_dpp v66, v66, v66 quad_perm:[2,3,0,1] row_mask:0xf bank_mask:0xf bound_ctrl:1
	v_add_f32_e32 v130, v130, v131
	v_fmamk_f32 v65, v130, 0xbc800000, v65
	v_add_f32_dpp v66, v66, v66 row_half_mirror row_mask:0xf bank_mask:0xf bound_ctrl:1
	v_fmamk_f32 v64, v130, 0xbc800000, v64
	v_fmamk_f32 v63, v130, 0xbc800000, v63
	v_fmamk_f32 v62, v130, 0xbc800000, v62
	v_fmamk_f32 v61, v130, 0xbc800000, v61
	v_fmamk_f32 v60, v130, 0xbc800000, v60
	v_fmamk_f32 v59, v130, 0xbc800000, v59
	v_fmamk_f32 v58, v130, 0xbc800000, v58
	v_fmamk_f32 v57, v130, 0xbc800000, v57
	v_fmamk_f32 v56, v130, 0xbc800000, v56
	v_fmamk_f32 v55, v130, 0xbc800000, v55
	v_fmamk_f32 v54, v130, 0xbc800000, v54
	v_fmamk_f32 v53, v130, 0xbc800000, v53
	v_fmamk_f32 v52, v130, 0xbc800000, v52
	v_fmamk_f32 v51, v130, 0xbc800000, v51
	v_fmac_f32_e32 v50, 0xbc800000, v130
	v_add_f32_dpp v66, v66, v66 row_ror:8 row_mask:0xf bank_mask:0xf bound_ctrl:1
	v_fmamk_f32 v17, v130, 0xbc800000, v17
	v_fmamk_f32 v16, v130, 0xbc800000, v16
	v_fmamk_f32 v15, v130, 0xbc800000, v15
	v_fmamk_f32 v14, v130, 0xbc800000, v14
	v_fmamk_f32 v13, v130, 0xbc800000, v13
	v_fmamk_f32 v12, v130, 0xbc800000, v12
	v_fmamk_f32 v11, v130, 0xbc800000, v11
	v_fmamk_f32 v10, v130, 0xbc800000, v10
	v_fmamk_f32 v9, v130, 0xbc800000, v9
	v_fmamk_f32 v8, v130, 0xbc800000, v8
	v_fmamk_f32 v7, v130, 0xbc800000, v7
	v_fmamk_f32 v6, v130, 0xbc800000, v6
	v_fmamk_f32 v5, v130, 0xbc800000, v5
	v_fmamk_f32 v4, v130, 0xbc800000, v4
	v_fmamk_f32 v3, v130, 0xbc800000, v3
	v_fmac_f32_e32 v2, 0xbc800000, v130
	v_pk_mul_f32 v[130:131], v[54:55], v[54:55]
	v_pk_mul_f32 v[132:133], v[62:63], v[62:63]
	v_pk_mul_f32 v[138:139], v[50:51], v[50:51]
	v_pk_mul_f32 v[140:141], v[58:59], v[58:59]
	v_pk_mul_f32 v[142:143], v[56:57], v[56:57]
	v_pk_mul_f32 v[144:145], v[64:65], v[64:65]
	v_pk_mul_f32 v[146:147], v[52:53], v[52:53]
	v_pk_mul_f32 v[148:149], v[60:61], v[60:61]
	v_mov_b32_e32 v67, v66
	v_pk_fma_f32 v[148:149], v[12:13], v[12:13], v[148:149]
	v_pk_fma_f32 v[146:147], v[4:5], v[4:5], v[146:147]
	v_pk_fma_f32 v[144:145], v[16:17], v[16:17], v[144:145]
	v_pk_fma_f32 v[142:143], v[8:9], v[8:9], v[142:143]
	v_pk_fma_f32 v[140:141], v[10:11], v[10:11], v[140:141]
	v_pk_fma_f32 v[138:139], v[2:3], v[2:3], v[138:139]
	v_pk_fma_f32 v[132:133], v[14:15], v[14:15], v[132:133]
	v_pk_fma_f32 v[130:131], v[6:7], v[6:7], v[130:131]
	v_permlane16_swap_b32_e32 v66, v67
	v_pk_add_f32 v[130:131], v[130:131], v[132:133]
	v_pk_add_f32 v[132:133], v[138:139], v[140:141]
	v_pk_add_f32 v[138:139], v[142:143], v[144:145]
	v_pk_add_f32 v[140:141], v[146:147], v[148:149]
	v_mfma_f32_32x32x16_bf16 v[18:33], v[74:77], v[78:81], v[18:33]
	v_add_f32_e32 v136, v66, v67
	ds_read_b128 v[70:73], v134 offset:512
	ds_read_b128 v[66:69], v134 offset:544
	ds_read_b128 v[78:81], v134 offset:576
	ds_read_b128 v[74:77], v134 offset:608
	ds_read_b128 v[82:85], v134 offset:640
	ds_read_b128 v[90:93], v134 offset:672
	ds_read_b128 v[86:89], v134 offset:704
	ds_read_b128 v[94:97], v134 offset:736
	v_pk_add_f32 v[138:139], v[140:141], v[138:139]
	v_pk_add_f32 v[130:131], v[132:133], v[130:131]
	s_waitcnt lgkmcnt(8)
	v_pk_mul_f32 v[140:141], v[126:127], v[62:63]
	v_pk_mov_b32 v[132:133], v[130:131], v[138:139] op_sel:[1,0]
	v_mov_b32_e32 v131, v139
	v_pk_mul_f32 v[138:139], v[122:123], v[54:55]
	v_pk_mul_f32 v[142:143], v[114:115], v[50:51]
	v_pk_mul_f32 v[144:145], v[118:119], v[58:59]
	v_pk_mul_f32 v[146:147], v[124:125], v[56:57]
	v_pk_mul_f32 v[148:149], v[128:129], v[64:65]
	v_pk_mul_f32 v[154:155], v[116:117], v[52:53]
	v_pk_mul_f32 v[156:157], v[120:121], v[60:61]
	v_pk_fma_f32 v[154:155], v[104:105], v[4:5], v[154:155]
	v_pk_fma_f32 v[156:157], v[112:113], v[12:13], v[156:157]
	v_pk_fma_f32 v[148:149], v[108:109], v[16:17], v[148:149]
	v_pk_fma_f32 v[146:147], v[100:101], v[8:9], v[146:147]
	v_pk_fma_f32 v[144:145], v[110:111], v[10:11], v[144:145]
	v_pk_fma_f32 v[142:143], v[102:103], v[2:3], v[142:143]
	v_pk_fma_f32 v[140:141], v[106:107], v[14:15], v[140:141]
	v_pk_fma_f32 v[138:139], v[98:99], v[6:7], v[138:139]
	v_pk_add_f32 v[130:131], v[132:133], v[130:131]
	v_pk_add_f32 v[138:139], v[138:139], v[140:141]
	v_pk_add_f32 v[140:141], v[142:143], v[144:145]
	v_pk_add_f32 v[142:143], v[146:147], v[148:149]
	v_pk_add_f32 v[144:145], v[154:155], v[156:157]
	v_pk_add_f32 v[132:133], v[130:131], v[130:131] op_sel:[0,1] op_sel_hi:[1,0]
	v_pk_add_f32 v[142:143], v[144:145], v[142:143]
	v_pk_add_f32 v[138:139], v[140:141], v[138:139]
	v_add_f32_e32 v133, v142, v143
	v_add_f32_e32 v130, v138, v139
	s_waitcnt lgkmcnt(2)
	v_pk_mul_f32 v[138:139], v[90:91], v[54:55]
	s_waitcnt lgkmcnt(0)
	v_pk_mul_f32 v[140:141], v[94:95], v[62:63]
	v_pk_mul_f32 v[142:143], v[82:83], v[50:51]
	v_pk_mul_f32 v[144:145], v[86:87], v[58:59]
	v_pk_mul_f32 v[146:147], v[92:93], v[56:57]
	v_pk_mul_f32 v[148:149], v[96:97], v[64:65]
	v_pk_mul_f32 v[154:155], v[84:85], v[52:53]
	v_pk_mul_f32 v[156:157], v[88:89], v[60:61]
	v_add_f32_e32 v130, v130, v133
	v_pk_fma_f32 v[156:157], v[80:81], v[12:13], v[156:157]
	v_pk_fma_f32 v[154:155], v[72:73], v[4:5], v[154:155]
	v_pk_fma_f32 v[148:149], v[76:77], v[16:17], v[148:149]
	v_pk_fma_f32 v[146:147], v[68:69], v[8:9], v[146:147]
	v_pk_fma_f32 v[144:145], v[78:79], v[10:11], v[144:145]
	v_pk_fma_f32 v[142:143], v[70:71], v[2:3], v[142:143]
	v_pk_fma_f32 v[140:141], v[74:75], v[14:15], v[140:141]
	v_pk_fma_f32 v[138:139], v[66:67], v[6:7], v[138:139]
	v_mov_b32_e32 v133, v130
	v_pk_add_f32 v[138:139], v[138:139], v[140:141]
	v_pk_add_f32 v[140:141], v[142:143], v[144:145]
	v_pk_add_f32 v[142:143], v[146:147], v[148:149]
	v_pk_add_f32 v[144:145], v[154:155], v[156:157]
	v_permlane32_swap_b32_e32 v130, v133
	v_pk_add_f32 v[142:143], v[144:145], v[142:143]
	v_add_f32_e32 v160, v130, v133
	v_pk_add_f32 v[138:139], v[140:141], v[138:139]
	v_add_f32_e32 v133, v142, v143
	v_pk_add_f32 v[140:141], v[26:27], v[42:43]
	v_pk_add_f32 v[142:143], v[28:29], v[44:45]
	v_pk_add_f32 v[144:145], v[20:21], v[36:37]
	v_pk_add_f32 v[146:147], v[32:33], v[48:49]
	v_pk_add_f32 v[148:149], v[24:25], v[40:41]
	v_pk_add_f32 v[154:155], v[30:31], v[46:47]
	v_pk_add_f32 v[156:157], v[22:23], v[38:39]
	v_pk_add_f32 v[158:159], v[18:19], v[34:35]
	v_pk_add_f32 v[154:155], v[156:157], v[154:155]
	v_pk_add_f32 v[146:147], v[148:149], v[146:147]
	v_pk_add_f32 v[142:143], v[144:145], v[142:143]
	v_pk_add_f32 v[140:141], v[158:159], v[140:141]
	v_pk_add_f32 v[142:143], v[142:143], v[146:147]
	v_pk_add_f32 v[140:141], v[140:141], v[154:155]
	v_add_f32_e32 v130, v138, v139
	v_pk_mov_b32 v[144:145], v[140:141], v[142:143] op_sel:[1,0]
	v_mov_b32_e32 v141, v143
	v_pk_add_f32 v[140:141], v[144:145], v[140:141]
	v_add_f32_e32 v133, v130, v133
	v_pk_add_f32 v[140:141], v[140:141], v[140:141] op_sel:[0,1] op_sel_hi:[1,0]
	v_mov_b32_e32 v131, v132
	v_mov_b32_e32 v130, v140
	s_nop 1
	v_permlane32_swap_b32_e32 v140, v130
	v_add_f32_e32 v130, v140, v130
	v_fmamk_f32 v49, v130, 0xbc800000, v49
	v_fmamk_f32 v48, v130, 0xbc800000, v48
	v_fmamk_f32 v47, v130, 0xbc800000, v47
	v_fmamk_f32 v46, v130, 0xbc800000, v46
	v_fmamk_f32 v45, v130, 0xbc800000, v45
	v_fmamk_f32 v44, v130, 0xbc800000, v44
	v_fmamk_f32 v43, v130, 0xbc800000, v43
	v_fmamk_f32 v42, v130, 0xbc800000, v42
	v_fmamk_f32 v41, v130, 0xbc800000, v41
	v_fmamk_f32 v40, v130, 0xbc800000, v40
	v_fmamk_f32 v39, v130, 0xbc800000, v39
	v_fmamk_f32 v38, v130, 0xbc800000, v38
	v_fmamk_f32 v37, v130, 0xbc800000, v37
	v_fmamk_f32 v36, v130, 0xbc800000, v36
	v_fmamk_f32 v35, v130, 0xbc800000, v35
	v_fmac_f32_e32 v34, 0xbc800000, v130
	v_fmamk_f32 v33, v130, 0xbc800000, v33
	v_fmamk_f32 v32, v130, 0xbc800000, v32
	v_fmamk_f32 v31, v130, 0xbc800000, v31
	v_fmamk_f32 v30, v130, 0xbc800000, v30
	v_fmamk_f32 v29, v130, 0xbc800000, v29
	v_fmamk_f32 v28, v130, 0xbc800000, v28
	v_fmamk_f32 v27, v130, 0xbc800000, v27
	v_fmamk_f32 v26, v130, 0xbc800000, v26
	v_fmamk_f32 v25, v130, 0xbc800000, v25
	v_fmamk_f32 v24, v130, 0xbc800000, v24
	v_fmamk_f32 v23, v130, 0xbc800000, v23
	v_fmamk_f32 v22, v130, 0xbc800000, v22
	v_fmamk_f32 v21, v130, 0xbc800000, v21
	v_fmamk_f32 v20, v130, 0xbc800000, v20
	v_fmamk_f32 v19, v130, 0xbc800000, v19
	v_fmac_f32_e32 v18, 0xbc800000, v130
	v_pk_mul_f32 v[140:141], v[38:39], v[38:39]
	v_pk_mul_f32 v[142:143], v[46:47], v[46:47]
	v_pk_mul_f32 v[144:145], v[34:35], v[34:35]
	v_pk_mul_f32 v[146:147], v[42:43], v[42:43]
	v_pk_mul_f32 v[148:149], v[40:41], v[40:41]
	v_pk_mul_f32 v[154:155], v[48:49], v[48:49]
	v_pk_mul_f32 v[156:157], v[36:37], v[36:37]
	v_pk_mul_f32 v[158:159], v[44:45], v[44:45]
	v_pk_fma_f32 v[156:157], v[20:21], v[20:21], v[156:157]
	v_pk_fma_f32 v[158:159], v[28:29], v[28:29], v[158:159]
	v_pk_fma_f32 v[154:155], v[32:33], v[32:33], v[154:155]
	v_pk_fma_f32 v[148:149], v[24:25], v[24:25], v[148:149]
	v_pk_fma_f32 v[146:147], v[26:27], v[26:27], v[146:147]
	v_pk_fma_f32 v[144:145], v[18:19], v[18:19], v[144:145]
	v_pk_fma_f32 v[142:143], v[30:31], v[30:31], v[142:143]
	v_pk_fma_f32 v[140:141], v[22:23], v[22:23], v[140:141]
	v_permlane32_swap_b32_e32 v132, v131
	v_pk_add_f32 v[140:141], v[140:141], v[142:143]
	v_pk_add_f32 v[142:143], v[144:145], v[146:147]
	v_pk_add_f32 v[144:145], v[148:149], v[154:155]
	v_pk_add_f32 v[146:147], v[156:157], v[158:159]
	v_pk_add_f32 v[140:141], v[142:143], v[140:141]
	v_pk_add_f32 v[144:145], v[146:147], v[144:145]
	v_pk_mul_f32 v[122:123], v[122:123], v[38:39]
	v_pk_mov_b32 v[142:143], v[140:141], v[144:145] op_sel:[1,0]
	v_mov_b32_e32 v141, v145
	v_pk_add_f32 v[140:141], v[142:143], v[140:141]
	v_pk_mul_f32 v[126:127], v[126:127], v[46:47]
	v_pk_add_f32 v[140:141], v[140:141], v[140:141] op_sel:[0,1] op_sel_hi:[1,0]
	v_pk_mul_f32 v[114:115], v[114:115], v[34:35]
	v_mov_b32_e32 v130, v140
	s_nop 1
	v_permlane32_swap_b32_e32 v140, v130
	v_mov_b32_e32 v141, v132
	v_pk_add_f32 v[130:131], v[140:141], v[130:131]
	v_pk_mul_f32 v[118:119], v[118:119], v[42:43]
	v_pk_fma_f32 v[130:131], v[130:131], s[0:1], v[152:153] op_sel_hi:[1,0,0]
	v_pk_mul_f32 v[124:125], v[124:125], v[40:41]
	v_mul_f32_e32 v132, 0x4b800000, v131
	v_cmp_gt_f32_e32 vcc, s1, v131
	v_pk_mul_f32 v[128:129], v[128:129], v[48:49]
	v_pk_mul_f32 v[116:117], v[116:117], v[36:37]
	v_pk_mul_f32 v[120:121], v[120:121], v[44:45]
	v_cndmask_b32_e32 v131, v131, v132, vcc
	v_mul_f32_e32 v132, 0x4b800000, v130
	v_cmp_gt_f32_e64 s[0:1], s1, v130
	v_pk_fma_f32 v[112:113], v[112:113], v[28:29], v[120:121]
	v_pk_fma_f32 v[104:105], v[104:105], v[20:21], v[116:117]
	v_pk_fma_f32 v[108:109], v[108:109], v[32:33], v[128:129]
	v_pk_fma_f32 v[100:101], v[100:101], v[24:25], v[124:125]
	v_pk_fma_f32 v[110:111], v[110:111], v[26:27], v[118:119]
	v_pk_fma_f32 v[102:103], v[102:103], v[18:19], v[114:115]
	v_pk_fma_f32 v[106:107], v[106:107], v[30:31], v[126:127]
	v_pk_fma_f32 v[98:99], v[98:99], v[22:23], v[122:123]
	v_rsq_f32_e32 v131, v131
	v_cndmask_b32_e64 v130, v130, v132, s[0:1]
	v_pk_add_f32 v[98:99], v[98:99], v[106:107]
	v_pk_add_f32 v[102:103], v[102:103], v[110:111]
	v_pk_add_f32 v[100:101], v[100:101], v[108:109]
	v_pk_add_f32 v[104:105], v[104:105], v[112:113]
	v_rsq_f32_e32 v132, v130
	v_pk_add_f32 v[100:101], v[104:105], v[100:101]
	v_pk_add_f32 v[98:99], v[102:103], v[98:99]
	v_mul_f32_e32 v130, 0x45800000, v131
	v_add_f32_e32 v98, v98, v99
	v_add_f32_e32 v99, v100, v101
	v_add_f32_e32 v98, v98, v99
	v_mov_b32_e32 v99, v98
	v_pk_mul_f32 v[90:91], v[90:91], v[38:39]
	v_pk_mul_f32 v[94:95], v[94:95], v[46:47]
	v_pk_mul_f32 v[82:83], v[82:83], v[34:35]
	v_pk_mul_f32 v[86:87], v[86:87], v[42:43]
	v_cndmask_b32_e32 v130, v131, v130, vcc
	v_mul_f32_e32 v131, 0x45800000, v132
	v_permlane32_swap_b32_e32 v98, v99
	v_pk_fma_f32 v[78:79], v[78:79], v[26:27], v[86:87]
	v_pk_fma_f32 v[70:71], v[70:71], v[18:19], v[82:83]
	v_pk_fma_f32 v[74:75], v[74:75], v[30:31], v[94:95]
	v_pk_fma_f32 v[66:67], v[66:67], v[22:23], v[90:91]
	v_cndmask_b32_e64 v131, v132, v131, s[0:1]
	v_add_f32_e32 v98, v98, v99
	v_pk_add_f32 v[66:67], v[66:67], v[74:75]
	v_pk_add_f32 v[70:71], v[70:71], v[78:79]
	v_mul_f32_e32 v139, v160, v130
	v_mul_f32_e32 v98, v98, v131
	v_pk_add_f32 v[66:67], v[70:71], v[66:67]
	v_cmp_gt_u32_e32 vcc, 32, v1
	v_add_f32_e32 v66, v66, v67
	v_pk_mul_f32 v[92:93], v[92:93], v[40:41]
	v_cndmask_b32_e32 v67, v98, v139, vcc
	v_add_f32_e32 v67, s12, v67
	v_pk_mul_f32 v[96:97], v[96:97], v[48:49]
	v_pk_mul_f32 v[84:85], v[84:85], v[36:37]
	v_pk_mul_f32 v[88:89], v[88:89], v[44:45]
	v_mul_f32_e32 v67, 0xbfb8aa3b, v67
	v_pk_fma_f32 v[80:81], v[80:81], v[28:29], v[88:89]
	v_pk_fma_f32 v[72:73], v[72:73], v[20:21], v[84:85]
	v_pk_fma_f32 v[76:77], v[76:77], v[32:33], v[96:97]
	v_pk_fma_f32 v[68:69], v[68:69], v[24:25], v[92:93]
	v_exp_f32_e32 v70, v67
	v_pk_add_f32 v[68:69], v[68:69], v[76:77]
	v_pk_add_f32 v[72:73], v[72:73], v[80:81]
	v_cmp_lt_i32_e64 s[0:1], 0, v151
	v_pk_add_f32 v[68:69], v[72:73], v[68:69]
	v_mov_b32_e32 v137, v136
	v_add_f32_e32 v67, v68, v69
	v_add_f32_e32 v67, v66, v67
	v_add_f32_e32 v66, 1.0, v70
	v_rcp_f32_e32 v66, v66
	v_mov_b32_e32 v69, 0xff800000
	v_mov_b32_e32 v138, v133
	v_mov_b32_e32 v68, v67
	v_cndmask_b32_e64 v70, v69, v66, s[0:1]
	v_mbcnt_lo_u32_b32 v66, -1, 0
	v_mbcnt_hi_u32_b32 v66, -1, v66
	v_permlane32_swap_b32_e32 v136, v137
	v_permlane32_swap_b32_e32 v133, v138
	v_permlane32_swap_b32_e32 v67, v68
	v_and_b32_e32 v86, 64, v66
	s_mov_b32 s14, 8
	s_mov_b32 s13, 0
	v_mov_b32_e32 v66, 0
	s_waitcnt lgkmcnt(0)
